# GLA chain step: LDS-DMA prefetch of the next stage issued ahead of the eight scattered silu(r) loads (in-order VMEM queue)
# speedup vs baseline: 1.0078x; 1.0078x over previous
; DI void gla_s_chain(LAS unsigned char* lds, const Ctx& c, int l, int bl, int h, int seg) {
;     ...
;     const unsigned lds_u = (unsigned)(uintptr_t)lds;
.LBB0_767:
	v_lshl_add_u64 v[78:79], s[30:31], 0, v[142:143]
	v_add_co_u32_e32 v78, vcc, 0x1c9c4000, v78
	s_waitcnt lgkmcnt(0)
	s_barrier
	s_nop 0
	v_addc_co_u32_e32 v79, vcc, 0, v79, vcc
	v_lshl_add_u64 v[144:145], s[30:31], 0, v[128:129]
	global_load_dword v218, v[78:79], off
	global_load_dword v217, v[78:79], off offset:256
	global_load_dword v216, v[78:79], off offset:512
	global_load_dword v215, v[78:79], off offset:768
	global_load_dword v214, v[78:79], off offset:1024
	global_load_dword v213, v[78:79], off offset:1280
	global_load_dword v212, v[78:79], off offset:1536
	global_load_dword v206, v[78:79], off offset:1792
	s_mov_b32 s53, 1
	s_cmp_eq_u32 s49, 15
	s_cbranch_scc1 .Lgs_nodma
	s_and_b32 s53, s49, 1
	s_xor_b32 s6, s53, 1
	s_mul_i32 s6, s6, 0x10400
	s_add_i32 s6, s6, s38
	v_lshl_add_u64 v[78:79], s[30:31], 0, v[140:141]
	s_mov_b64 s[8:9], 0x46bd0800
	s_add_i32 s7, s6, s48
	v_lshl_add_u64 v[80:81], v[78:79], 0, s[8:9]
	s_mov_b32 s8, m0
	s_mov_b32 m0, s7
	s_nop 0
	global_load_lds_dwordx4 v[80:81], off
	s_mov_b32 m0, s8
	s_mov_b64 s[8:9], 0x46bd0c00
	s_add_i32 s7, s6, s5
	v_lshl_add_u64 v[80:81], v[78:79], 0, s[8:9]
	s_mov_b32 s8, m0
	s_mov_b32 m0, s7
	s_nop 0
	global_load_lds_dwordx4 v[80:81], off
	s_mov_b32 m0, s8
	s_mov_b64 s[8:9], 0x46bd1000
	s_add_i32 s7, s6, s85
	v_lshl_add_u64 v[80:81], v[78:79], 0, s[8:9]
	s_mov_b32 s8, m0
	s_mov_b32 m0, s7
	s_nop 0
	global_load_lds_dwordx4 v[80:81], off
	s_mov_b32 m0, s8
	s_mov_b64 s[8:9], 0x46bd1400
	s_add_i32 s7, s6, s86
	v_lshl_add_u64 v[78:79], v[78:79], 0, s[8:9]
	s_mov_b32 s8, m0
	s_mov_b32 m0, s7
	s_nop 0
	global_load_lds_dwordx4 v[78:79], off
	s_mov_b32 m0, s8
	s_and_b64 vcc, exec, s[40:41]
	s_cbranch_vccnz .LBB0_770
	v_lshl_add_u64 v[78:79], s[30:31], 0, v[138:139]
	s_add_i32 s7, s6, 0x8000
	s_mov_b32 s8, m0
	s_mov_b32 m0, s7
	s_nop 0
	global_load_lds_dwordx4 v[78:79], off
	s_mov_b32 m0, s8

.Lgs_nodma:
	v_add_co_u32_e32 v78, vcc, 0x28bc0000, v144
	s_nop 1
	v_addc_co_u32_e32 v79, vcc, 0, v145, vcc
	global_load_dword v197, v[78:79], off
	global_load_dword v196, v[78:79], off offset:16
	v_add_co_u32_e32 v78, vcc, 0x28bc4000, v144
	s_nop 0
	s_nop 0
	v_addc_co_u32_e32 v79, vcc, 0, v145, vcc
	global_load_dword v195, v[78:79], off
	global_load_dword v194, v[78:79], off offset:16
	v_add_co_u32_e32 v78, vcc, 0x28bc8000, v144
	s_nop 1
	v_addc_co_u32_e32 v79, vcc, 0, v145, vcc
	global_load_dword v193, v[78:79], off
	global_load_dword v192, v[78:79], off offset:16
	v_add_co_u32_e32 v78, vcc, 0x28bcc000, v144
	s_nop 1
	v_addc_co_u32_e32 v79, vcc, 0, v145, vcc
	global_load_dword v191, v[78:79], off
	global_load_dword v127, v[78:79], off offset:16
